# fnet fold units: one L2 write-back by the publishing lane after the workgroup barrier instead of one per wave (plus earlier edits)
# speedup vs baseline: 1.0109x; 1.0109x over previous
.LBB0_672:
	s_or_b64 exec, exec, s[6:7]
	s_waitcnt vmcnt(0) lgkmcnt(0)
	s_barrier
	s_and_saveexec_b64 s[4:5], s[20:21]
	s_cbranch_execz .LBB0_675
	s_mov_b64 s[6:7], exec
	v_mbcnt_lo_u32_b32 v2, s6, 0
	v_mbcnt_hi_u32_b32 v2, s7, v2
	v_cmp_eq_u32_e32 vcc, 0, v2
	s_and_b64 s[10:11], exec, vcc
	s_mov_b64 exec, s[10:11]
	s_cbranch_execz .LBB0_675
	s_ashr_i32 s1, s57, 31
	s_add_u32 s10, s37, s57
	s_addc_u32 s11, 0, s1
	s_lshl_b64 s[10:11], s[10:11], 2
	s_add_u32 s10, s72, s10
	s_addc_u32 s11, s73, s11
	s_bcnt1_i32_b64 s1, s[6:7]
	v_mov_b32_e32 v2, s1
	buffer_wbl2 sc1
	s_waitcnt vmcnt(0)
	global_atomic_add v131, v2, s[10:11] offset:-608

.LBB0_794:
	s_or_b64 exec, exec, s[8:9]
	s_waitcnt vmcnt(0) lgkmcnt(0)
	s_barrier
	s_and_saveexec_b64 s[4:5], s[20:21]
	s_cbranch_execz .LBB0_797
	s_mov_b64 s[8:9], exec
	v_mbcnt_lo_u32_b32 v2, s8, 0
	v_mbcnt_hi_u32_b32 v2, s9, v2
	v_cmp_eq_u32_e32 vcc, 0, v2
	s_and_b64 s[10:11], exec, vcc
	s_mov_b64 exec, s[10:11]
	s_cbranch_execz .LBB0_797
	s_lshl_b64 s[6:7], s[6:7], 2
	s_add_u32 s6, s72, s6
	s_addc_u32 s7, s73, s7
	s_bcnt1_i32_b64 s1, s[8:9]
	v_mov_b32_e32 v2, s1
	buffer_wbl2 sc1
	s_waitcnt vmcnt(0)
	global_atomic_add v131, v2, s[6:7]
